# P1: non-temporal hint on the streaming x loads
# speedup vs baseline: 1.0720x; 1.0071x over previous
.LBB0_103:
	s_ashr_i32 s17, s16, 31
	s_lshl_b64 s[20:21], s[16:17], 12
	s_ashr_i32 s17, s40, 6
	s_mul_hi_i32 s23, s17, 0x6000
	v_lshlrev_b32_e32 v114, 2, v1
	s_mulk_i32 s17, 0x6000
	s_add_u32 s22, s10, s17
	v_ashrrev_i32_e32 v115, 31, v114
	s_addc_u32 s23, s11, s23
	v_lshlrev_b64 v[116:117], 2, v[114:115]
	s_waitcnt vmcnt(31)
	v_lshl_add_u64 v[2:3], s[22:23], 0, v[116:117]
	v_add_co_u32_e32 v4, vcc, s26, v2
	s_lshl_b32 s42, s40, 5
	s_nop 0
	v_addc_co_u32_e32 v5, vcc, 0, v3, vcc
	s_waitcnt vmcnt(30)
	v_add_co_u32_e32 v6, vcc, s30, v2
	global_load_dwordx4 v[66:69], v[2:3], off
	s_nop 0
	v_addc_co_u32_e32 v7, vcc, 0, v3, vcc
	v_add_co_u32_e32 v8, vcc, s27, v2
	global_load_dwordx4 v[70:73], v[6:7], off offset:-4096
	s_nop 0
	v_addc_co_u32_e32 v9, vcc, 0, v3, vcc
	s_waitcnt vmcnt(31)
	v_add_co_u32_e32 v10, vcc, s31, v2
	s_ashr_i32 s43, s42, 31
	s_nop 0
	v_addc_co_u32_e32 v11, vcc, 0, v3, vcc
	v_add_co_u32_e32 v12, vcc, s28, v2
	global_load_dwordx4 v[74:77], v[10:11], off offset:-4096
	s_nop 0
	v_addc_co_u32_e32 v13, vcc, 0, v3, vcc
	s_waitcnt vmcnt(31)
	v_add_co_u32_e32 v14, vcc, s34, v2
	s_lshl_b64 s[22:23], s[42:43], 10
	s_nop 0
	v_addc_co_u32_e32 v15, vcc, 0, v3, vcc
	v_add_co_u32_e32 v16, vcc, s29, v2
	global_load_dwordx4 v[78:81], v[14:15], off offset:-4096
	s_nop 0
	v_addc_co_u32_e32 v17, vcc, 0, v3, vcc
	global_load_dwordx4 v[82:85], v[16:17], off
	global_load_dwordx4 v[86:89], v[6:7], off
	global_load_dwordx4 v[90:93], v[10:11], off
	global_load_dwordx4 v[94:97], v[14:15], off
	global_load_dwordx4 v[98:101], v[2:3], off offset:1024
	global_load_dwordx4 v[106:109], v[4:5], off offset:1024
	global_load_dwordx4 v[118:121], v[8:9], off offset:1024
	global_load_dwordx4 v[122:125], v[12:13], off offset:1024
	s_lshl_b64 s[42:43], s[42:43], 12
	s_add_u32 s42, s6, s42
	s_addc_u32 s43, s7, s43
	s_waitcnt vmcnt(36)
	v_lshl_add_u64 v[30:31], s[42:43], 0, v[116:117]
	v_add_co_u32_e32 v32, vcc, s29, v30
	v_lshl_add_u64 v[18:19], s[8:9], 0, v[116:117]
	s_nop 0
	v_addc_co_u32_e32 v33, vcc, 0, v31, vcc
	v_lshl_add_u64 v[20:21], s[14:15], 0, v[116:117]
	global_load_dwordx4 v[110:113], v[18:19], off
	global_load_dwordx4 v[102:105], v[18:19], off offset:1024
	global_load_dwordx4 v[126:129], v[16:17], off offset:1024
	global_load_dwordx4 v[138:141], v[10:11], off offset:1024
	global_load_dwordx4 v[134:137], v[20:21], off
	global_load_dwordx4 v[142:145], v[20:21], off offset:1024
	global_load_dwordx4 v[146:149], v[4:5], off offset:2048
	global_load_dwordx4 v[150:153], v[12:13], off offset:2048
	global_load_dwordx4 v[154:157], v[4:5], off offset:3072
	global_load_dwordx4 v[158:161], v[6:7], off offset:3072
	global_load_dwordx4 v[162:165], v[6:7], off offset:1024
	global_load_dwordx4 v[170:173], v[6:7], off offset:2048
	global_load_dwordx4 v[174:177], v[14:15], off offset:1024
	global_load_dwordx4 v[178:181], v[14:15], off offset:2048
	global_load_dwordx4 v[182:185], v[2:3], off offset:2048
	global_load_dwordx4 v[186:189], v[2:3], off offset:3072
	global_load_dwordx4 v[190:193], v[18:19], off offset:2048
	global_load_dwordx4 v[194:197], v[18:19], off offset:3072
	global_load_dwordx4 v[198:201], v[8:9], off offset:2048
	global_load_dwordx4 v[202:205], v[8:9], off offset:3072
	global_load_dwordx4 v[206:209], v[12:13], off offset:3072
	global_load_dwordx4 v[210:213], v[20:21], off offset:2048
	global_load_dwordx4 v[214:217], v[20:21], off offset:3072
	global_load_dwordx4 v[218:221], v[16:17], off offset:2048
	global_load_dwordx4 v[222:225], v[16:17], off offset:3072
	global_load_dwordx4 v[226:229], v[10:11], off offset:2048
	global_load_dwordx4 v[230:233], v[10:11], off offset:3072
	global_load_dwordx4 v[234:237], v[14:15], off offset:3072
	s_waitcnt vmcnt(60)
	v_add_co_u32_e32 v46, vcc, s35, v30
	global_load_dwordx4 v[2:5], v[30:31], off nt
	global_load_dwordx4 v[6:9], v[30:31], off offset:1024 nt
	global_load_dwordx4 v[10:13], v[30:31], off offset:2048 nt
	global_load_dwordx4 v[14:17], v[30:31], off offset:3072 nt
	v_addc_co_u32_e32 v47, vcc, 0, v31, vcc
	global_load_dwordx4 v[18:21], v[32:33], off offset:1024 nt
	global_load_dwordx4 v[26:29], v[32:33], off offset:2048 nt
	global_load_dwordx4 v[22:25], v[46:47], off offset:-4096 nt
	global_load_dwordx4 v[34:37], v[46:47], off nt
	global_load_dwordx4 v[38:41], v[46:47], off offset:1024 nt
	global_load_dwordx4 v[42:45], v[46:47], off offset:2048 nt
	s_nop 0
	global_load_dwordx4 v[46:49], v[46:47], off offset:3072 nt
	s_waitcnt vmcnt(62)
	v_add_co_u32_e32 v62, vcc, 0x3000, v30
	s_add_u32 s22, s0, s22
	s_nop 0
	v_addc_co_u32_e32 v63, vcc, 0, v31, vcc
	global_load_dwordx4 v[30:33], v[32:33], off offset:3072 nt
	s_nop 0
	global_load_dwordx4 v[50:53], v[62:63], off nt
	global_load_dwordx4 v[54:57], v[62:63], off offset:1024 nt
	global_load_dwordx4 v[58:61], v[62:63], off offset:2048 nt
	s_nop 0
	global_load_dwordx4 v[62:65], v[62:63], off offset:3072 nt
	s_addc_u32 s23, s1, s23
	s_add_u32 s20, s6, s20
	s_addc_u32 s21, s7, s21
	s_waitcnt vmcnt(54)
	v_pk_add_f32 v[68:69], v[68:69], v[72:73]
	v_pk_add_f32 v[66:67], v[66:67], v[70:71]
	s_waitcnt vmcnt(52)
	v_pk_add_f32 v[70:71], v[76:77], v[80:81]
	v_pk_add_f32 v[72:73], v[74:75], v[78:79]
	s_waitcnt vmcnt(50)
	v_pk_add_f32 v[74:75], v[84:85], v[88:89]
	v_pk_add_f32 v[76:77], v[82:83], v[86:87]
	s_waitcnt vmcnt(48)
	v_pk_add_f32 v[78:79], v[92:93], v[96:97]
	v_pk_add_f32 v[80:81], v[90:91], v[94:95]
	s_waitcnt vmcnt(46)
	v_pk_add_f32 v[82:83], v[100:101], v[108:109]
	v_pk_add_f32 v[84:85], v[98:99], v[106:107]
	s_waitcnt vmcnt(44)
	v_pk_add_f32 v[86:87], v[120:121], v[124:125]
	v_pk_add_f32 v[88:89], v[118:119], v[122:123]
	v_pk_add_f32 v[68:69], v[68:69], v[70:71]
	v_pk_add_f32 v[66:67], v[66:67], v[72:73]
	v_pk_add_f32 v[70:71], v[74:75], v[78:79]
	v_pk_add_f32 v[72:73], v[76:77], v[80:81]
	v_pk_add_f32 v[74:75], v[82:83], v[86:87]
	v_pk_add_f32 v[76:77], v[84:85], v[88:89]
	s_waitcnt vmcnt(43)
	v_pk_add_f32 v[130:131], v[112:113], v[68:69]
	v_pk_add_f32 v[132:133], v[110:111], v[66:67]
	s_waitcnt vmcnt(39)
	v_pk_add_f32 v[66:67], v[136:137], v[70:71]
	v_pk_add_f32 v[68:69], v[134:135], v[72:73]
	v_pk_add_f32 v[134:135], v[104:105], v[74:75]
	v_pk_add_f32 v[136:137], v[102:103], v[76:77]
	s_waitcnt vmcnt(33)
	v_pk_add_f32 v[70:71], v[128:129], v[164:165]
	v_pk_add_f32 v[72:73], v[126:127], v[162:163]
	s_waitcnt vmcnt(31)
	v_pk_add_f32 v[74:75], v[140:141], v[176:177]
	v_pk_add_f32 v[76:77], v[138:139], v[174:175]
	v_pk_add_f32 v[70:71], v[70:71], v[74:75]
	v_pk_add_f32 v[72:73], v[72:73], v[76:77]
	s_waitcnt vmcnt(29)
	v_pk_add_f32 v[74:75], v[184:185], v[148:149]
	v_pk_add_f32 v[76:77], v[182:183], v[146:147]
	v_pk_add_f32 v[138:139], v[66:67], 1.0 op_sel_hi:[1,0]
	v_pk_add_f32 v[140:141], v[68:69], 1.0 op_sel_hi:[1,0]
	s_waitcnt vmcnt(25)
	v_pk_add_f32 v[66:67], v[200:201], v[152:153]
	v_pk_add_f32 v[68:69], v[198:199], v[150:151]
	v_pk_add_f32 v[70:71], v[144:145], v[70:71]
	v_pk_add_f32 v[72:73], v[142:143], v[72:73]
	v_pk_add_f32 v[66:67], v[74:75], v[66:67]
	v_pk_add_f32 v[68:69], v[76:77], v[68:69]
	v_pk_add_f32 v[142:143], v[70:71], 1.0 op_sel_hi:[1,0]
	v_pk_add_f32 v[144:145], v[72:73], 1.0 op_sel_hi:[1,0]
	v_pk_add_f32 v[146:147], v[192:193], v[66:67]
	v_pk_add_f32 v[148:149], v[190:191], v[68:69]
	s_waitcnt vmcnt(20)
	v_pk_add_f32 v[66:67], v[220:221], v[172:173]
	v_pk_add_f32 v[68:69], v[218:219], v[170:171]
	s_waitcnt vmcnt(18)
	v_pk_add_f32 v[70:71], v[228:229], v[180:181]
	v_pk_add_f32 v[72:73], v[226:227], v[178:179]
	v_pk_add_f32 v[66:67], v[66:67], v[70:71]
	v_pk_add_f32 v[68:69], v[68:69], v[72:73]
	v_pk_add_f32 v[66:67], v[212:213], v[66:67]
	v_pk_add_f32 v[68:69], v[210:211], v[68:69]
	v_pk_add_f32 v[150:151], v[66:67], 1.0 op_sel_hi:[1,0]
	v_pk_add_f32 v[152:153], v[68:69], 1.0 op_sel_hi:[1,0]
	v_pk_add_f32 v[66:67], v[188:189], v[156:157]
	v_pk_add_f32 v[68:69], v[186:187], v[154:155]
	v_pk_add_f32 v[70:71], v[204:205], v[208:209]
	v_pk_add_f32 v[72:73], v[202:203], v[206:207]
	v_pk_add_f32 v[66:67], v[66:67], v[70:71]
	v_pk_add_f32 v[68:69], v[68:69], v[72:73]
	v_pk_add_f32 v[154:155], v[196:197], v[66:67]
	v_pk_add_f32 v[156:157], v[194:195], v[68:69]
	v_pk_add_f32 v[66:67], v[224:225], v[160:161]
	v_pk_add_f32 v[68:69], v[222:223], v[158:159]
	s_waitcnt vmcnt(16)
	v_pk_add_f32 v[70:71], v[232:233], v[236:237]
	v_pk_add_f32 v[72:73], v[230:231], v[234:235]
	v_pk_add_f32 v[66:67], v[66:67], v[70:71]
	v_pk_add_f32 v[68:69], v[68:69], v[72:73]
	v_pk_add_f32 v[66:67], v[216:217], v[66:67]
	v_pk_add_f32 v[68:69], v[214:215], v[68:69]
	v_pk_add_f32 v[158:159], v[66:67], 1.0 op_sel_hi:[1,0]
	v_pk_add_f32 v[160:161], v[68:69], 1.0 op_sel_hi:[1,0]
	v_lshl_add_u64 v[162:163], s[22:23], 0, v[114:115]
	v_lshl_add_u64 v[164:165], s[20:21], 0, v[116:117]
	s_mov_b64 s[20:21], 0
	s_branch .LBB0_105

.LBB0_105:
	v_lshl_add_u64 v[166:167], v[164:165], 0, s[20:21]
	v_add_co_u32_e32 v66, vcc, s36, v166
	s_nop 1
	v_addc_co_u32_e32 v67, vcc, 0, v167, vcc
	v_add_co_u32_e32 v68, vcc, s37, v166
	s_nop 1
	v_addc_co_u32_e32 v69, vcc, 0, v167, vcc
	v_add_co_u32_e32 v70, vcc, s25, v166
	global_load_dwordx4 v[122:125], v[66:67], off offset:1024 nt
	global_load_dwordx4 v[114:117], v[66:67], off offset:2048 nt
	global_load_dwordx4 v[126:129], v[68:69], off offset:-4096 nt
	global_load_dwordx4 v[110:113], v[68:69], off nt
	global_load_dwordx4 v[106:109], v[68:69], off offset:1024 nt
	global_load_dwordx4 v[102:105], v[68:69], off offset:2048 nt
	v_addc_co_u32_e32 v71, vcc, 0, v167, vcc
	v_add_co_u32_e32 v170, vcc, s38, v166
	s_nop 1
	v_addc_co_u32_e32 v171, vcc, 0, v167, vcc
	global_load_dwordx4 v[98:101], v[68:69], off offset:3072 nt
	global_load_dwordx4 v[94:97], v[170:171], off offset:-4096 nt
	global_load_dwordx4 v[118:121], v[66:67], off offset:3072 nt
	global_load_dwordx4 v[90:93], v[70:71], off offset:1024 nt
	global_load_dwordx4 v[86:89], v[70:71], off offset:2048 nt
	global_load_dwordx4 v[82:85], v[70:71], off offset:3072 nt
	global_load_dwordx4 v[78:81], v[170:171], off nt
	global_load_dwordx4 v[74:77], v[170:171], off offset:1024 nt
	s_nop 0
	global_load_dwordx4 v[70:73], v[170:171], off offset:2048 nt
	global_load_dwordx4 v[66:69], v[170:171], off offset:3072 nt
	s_waitcnt vmcnt(31)
	v_fma_f32 v169, v140, v2, v132
	v_fma_f32 v170, v141, v3, v133
	v_med3_f32 v169, v169, s39, v168
	v_med3_f32 v170, v170, s39, v168
	v_mov_b32_e32 v172, 0
	v_cvt_pk_fp8_f32 v172, v169, v170
	v_fma_f32 v171, v138, v4, v130
	v_fma_f32 v169, v139, v5, v131
	v_med3_f32 v170, v171, s39, v168
	v_med3_f32 v169, v169, s39, v168
	v_cvt_pk_fp8_f32 v172, v170, v169 op_sel:[0,0,1]
	s_waitcnt vmcnt(30)
	v_fma_f32 v169, v144, v6, v136
	v_fma_f32 v170, v145, v7, v137
	v_med3_f32 v169, v169, s39, v168
	v_med3_f32 v170, v170, s39, v168
	v_mov_b32_e32 v173, 0
	v_cvt_pk_fp8_f32 v173, v169, v170
	v_fma_f32 v171, v142, v8, v134
	v_fma_f32 v169, v143, v9, v135
	v_med3_f32 v170, v171, s39, v168
	v_med3_f32 v169, v169, s39, v168
	v_cvt_pk_fp8_f32 v173, v170, v169 op_sel:[0,0,1]
	s_waitcnt vmcnt(29)
	v_fma_f32 v169, v152, v10, v148
	v_fma_f32 v170, v153, v11, v149
	v_med3_f32 v169, v169, s39, v168
	v_med3_f32 v170, v170, s39, v168
	v_mov_b32_e32 v174, 0
	v_cvt_pk_fp8_f32 v174, v169, v170
	v_fma_f32 v171, v150, v12, v146
	v_fma_f32 v169, v151, v13, v147
	v_med3_f32 v170, v171, s39, v168
	v_med3_f32 v169, v169, s39, v168
	v_cvt_pk_fp8_f32 v174, v170, v169 op_sel:[0,0,1]
	s_waitcnt vmcnt(28)
	v_fma_f32 v169, v160, v14, v156
	v_fma_f32 v170, v161, v15, v157
	v_med3_f32 v169, v169, s39, v168
	v_med3_f32 v170, v170, s39, v168
	v_mov_b32_e32 v175, 0
	v_cvt_pk_fp8_f32 v175, v169, v170
	v_fma_f32 v171, v158, v16, v154
	v_fma_f32 v169, v159, v17, v155
	v_med3_f32 v170, v171, s39, v168
	v_med3_f32 v169, v169, s39, v168
	v_cvt_pk_fp8_f32 v175, v170, v169 op_sel:[0,0,1]
	s_waitcnt vmcnt(25)
	v_fma_f32 v169, v140, v22, v132
	v_fma_f32 v170, v141, v23, v133
	global_store_dword v[162:163], v172, off
	global_store_dword v[162:163], v173, off offset:256
	global_store_dword v[162:163], v174, off offset:512
	global_store_dword v[162:163], v175, off offset:768
	v_med3_f32 v169, v169, s39, v168
	v_med3_f32 v170, v170, s39, v168
	v_mov_b32_e32 v172, 0
	v_cvt_pk_fp8_f32 v172, v169, v170
	v_fma_f32 v171, v138, v24, v130
	v_fma_f32 v169, v139, v25, v131
	v_med3_f32 v170, v171, s39, v168
	v_med3_f32 v169, v169, s39, v168
	v_cvt_pk_fp8_f32 v172, v170, v169 op_sel:[0,0,1]
	v_fma_f32 v169, v144, v18, v136
	v_fma_f32 v170, v145, v19, v137
	v_med3_f32 v169, v169, s39, v168
	v_med3_f32 v170, v170, s39, v168
	v_mov_b32_e32 v173, 0
	v_cvt_pk_fp8_f32 v173, v169, v170
	v_fma_f32 v171, v142, v20, v134
	v_fma_f32 v169, v143, v21, v135
	v_med3_f32 v170, v171, s39, v168
	v_med3_f32 v169, v169, s39, v168
	v_cvt_pk_fp8_f32 v173, v170, v169 op_sel:[0,0,1]
	v_fma_f32 v169, v152, v26, v148
	v_fma_f32 v170, v153, v27, v149
	v_med3_f32 v169, v169, s39, v168
	v_med3_f32 v170, v170, s39, v168
	v_mov_b32_e32 v174, 0
	v_cvt_pk_fp8_f32 v174, v169, v170
	v_fma_f32 v171, v150, v28, v146
	v_fma_f32 v169, v151, v29, v147
	v_med3_f32 v170, v171, s39, v168
	v_med3_f32 v169, v169, s39, v168
	v_cvt_pk_fp8_f32 v174, v170, v169 op_sel:[0,0,1]
	s_waitcnt vmcnt(24)
	v_fma_f32 v169, v160, v30, v156
	v_fma_f32 v170, v161, v31, v157
	v_med3_f32 v169, v169, s39, v168
	v_med3_f32 v170, v170, s39, v168
	v_mov_b32_e32 v175, 0
	v_cvt_pk_fp8_f32 v175, v169, v170
	v_fma_f32 v171, v158, v32, v154
	v_fma_f32 v169, v159, v33, v155
	v_med3_f32 v170, v171, s39, v168
	v_med3_f32 v169, v169, s39, v168
	v_cvt_pk_fp8_f32 v175, v170, v169 op_sel:[0,0,1]
	v_fma_f32 v169, v140, v34, v132
	v_fma_f32 v170, v141, v35, v133
	global_store_dword v[162:163], v172, off offset:1024
	global_store_dword v[162:163], v173, off offset:1280
	global_store_dword v[162:163], v174, off offset:1536
	global_store_dword v[162:163], v175, off offset:1792
	v_med3_f32 v169, v169, s39, v168
	v_med3_f32 v170, v170, s39, v168
	v_mov_b32_e32 v172, 0
	v_cvt_pk_fp8_f32 v172, v169, v170
	v_fma_f32 v171, v138, v36, v130
	v_fma_f32 v169, v139, v37, v131
	v_med3_f32 v170, v171, s39, v168
	v_med3_f32 v169, v169, s39, v168
	v_cvt_pk_fp8_f32 v172, v170, v169 op_sel:[0,0,1]
	v_fma_f32 v169, v144, v38, v136
	v_fma_f32 v170, v145, v39, v137
	v_med3_f32 v169, v169, s39, v168
	v_med3_f32 v170, v170, s39, v168
	v_mov_b32_e32 v173, 0
	v_cvt_pk_fp8_f32 v173, v169, v170
	v_fma_f32 v171, v142, v40, v134
	v_fma_f32 v169, v143, v41, v135
	v_med3_f32 v170, v171, s39, v168
	v_med3_f32 v169, v169, s39, v168
	v_cvt_pk_fp8_f32 v173, v170, v169 op_sel:[0,0,1]
	v_fma_f32 v169, v152, v42, v148
	v_fma_f32 v170, v153, v43, v149
	v_med3_f32 v169, v169, s39, v168
	v_med3_f32 v170, v170, s39, v168
	v_mov_b32_e32 v174, 0
	v_cvt_pk_fp8_f32 v174, v169, v170
	v_fma_f32 v171, v150, v44, v146
	v_fma_f32 v169, v151, v45, v147
	v_med3_f32 v170, v171, s39, v168
	v_med3_f32 v169, v169, s39, v168
	v_cvt_pk_fp8_f32 v174, v170, v169 op_sel:[0,0,1]
	v_fma_f32 v169, v160, v46, v156
	v_fma_f32 v170, v161, v47, v157
	v_med3_f32 v169, v169, s39, v168
	v_med3_f32 v170, v170, s39, v168
	v_mov_b32_e32 v175, 0
	v_cvt_pk_fp8_f32 v175, v169, v170
	v_fma_f32 v171, v158, v48, v154
	v_fma_f32 v169, v159, v49, v155
	v_med3_f32 v170, v171, s39, v168
	v_med3_f32 v169, v169, s39, v168
	v_cvt_pk_fp8_f32 v175, v170, v169 op_sel:[0,0,1]
	s_waitcnt vmcnt(27)
	v_fma_f32 v169, v140, v50, v132
	v_fma_f32 v170, v141, v51, v133
	global_store_dword v[162:163], v172, off offset:2048
	global_store_dword v[162:163], v173, off offset:2304
	global_store_dword v[162:163], v174, off offset:2560
	global_store_dword v[162:163], v175, off offset:2816
	v_med3_f32 v169, v169, s39, v168
	v_med3_f32 v170, v170, s39, v168
	v_mov_b32_e32 v172, 0
	v_cvt_pk_fp8_f32 v172, v169, v170
	v_fma_f32 v171, v138, v52, v130
	v_fma_f32 v169, v139, v53, v131
	v_med3_f32 v170, v171, s39, v168
	v_med3_f32 v169, v169, s39, v168
	v_cvt_pk_fp8_f32 v172, v170, v169 op_sel:[0,0,1]
	s_waitcnt vmcnt(30)
	v_fma_f32 v169, v144, v54, v136
	v_fma_f32 v170, v145, v55, v137
	v_med3_f32 v169, v169, s39, v168
	v_med3_f32 v170, v170, s39, v168
	v_mov_b32_e32 v173, 0
	v_cvt_pk_fp8_f32 v173, v169, v170
	v_fma_f32 v171, v142, v56, v134
	v_fma_f32 v169, v143, v57, v135
	v_med3_f32 v170, v171, s39, v168
	v_med3_f32 v169, v169, s39, v168
	v_cvt_pk_fp8_f32 v173, v170, v169 op_sel:[0,0,1]
	s_waitcnt vmcnt(29)
	v_fma_f32 v169, v152, v58, v148
	v_fma_f32 v170, v153, v59, v149
	v_med3_f32 v169, v169, s39, v168
	v_med3_f32 v170, v170, s39, v168
	v_mov_b32_e32 v174, 0
	v_cvt_pk_fp8_f32 v174, v169, v170
	v_fma_f32 v171, v150, v60, v146
	v_fma_f32 v169, v151, v61, v147
	v_med3_f32 v170, v171, s39, v168
	v_med3_f32 v169, v169, s39, v168
	v_cvt_pk_fp8_f32 v174, v170, v169 op_sel:[0,0,1]
	s_waitcnt vmcnt(28)
	v_fma_f32 v169, v160, v62, v156
	v_fma_f32 v170, v161, v63, v157
	v_med3_f32 v169, v169, s39, v168
	v_med3_f32 v170, v170, s39, v168
	v_mov_b32_e32 v175, 0
	v_cvt_pk_fp8_f32 v175, v169, v170
	v_fma_f32 v171, v158, v64, v154
	v_fma_f32 v169, v159, v65, v155
	v_med3_f32 v170, v171, s39, v168
	v_med3_f32 v169, v169, s39, v168
	v_cvt_pk_fp8_f32 v175, v170, v169 op_sel:[0,0,1]
	global_store_dword v[162:163], v172, off offset:3072
	global_store_dword v[162:163], v173, off offset:3328
	global_store_dword v[162:163], v174, off offset:3584
	global_store_dword v[162:163], v175, off offset:3840
	s_cmp_lg_u32 s20, 0x18000
	s_cbranch_scc0 .LBB0_104
	v_add_co_u32_e32 v14, vcc, 0x8000, v166
	s_nop 1
	v_addc_co_u32_e32 v15, vcc, 0, v167, vcc
	v_add_co_u32_e32 v30, vcc, 0x9000, v166
	global_load_dwordx4 v[2:5], v[14:15], off nt
	global_load_dwordx4 v[6:9], v[14:15], off offset:1024 nt
	global_load_dwordx4 v[10:13], v[14:15], off offset:2048 nt
	s_nop 0
	global_load_dwordx4 v[14:17], v[14:15], off offset:3072 nt
	v_addc_co_u32_e32 v31, vcc, 0, v167, vcc
	v_add_co_u32_e32 v46, vcc, 0xa000, v166
	global_load_dwordx4 v[22:25], v[30:31], off nt
	global_load_dwordx4 v[18:21], v[30:31], off offset:1024 nt
	global_load_dwordx4 v[26:29], v[30:31], off offset:2048 nt
	s_nop 0
	global_load_dwordx4 v[30:33], v[30:31], off offset:3072 nt
	v_addc_co_u32_e32 v47, vcc, 0, v167, vcc
	v_add_co_u32_e32 v62, vcc, 0xb000, v166
	global_load_dwordx4 v[34:37], v[46:47], off nt
	global_load_dwordx4 v[38:41], v[46:47], off offset:1024 nt
	global_load_dwordx4 v[42:45], v[46:47], off offset:2048 nt
	s_nop 0
	global_load_dwordx4 v[46:49], v[46:47], off offset:3072 nt
	v_addc_co_u32_e32 v63, vcc, 0, v167, vcc
	global_load_dwordx4 v[50:53], v[62:63], off nt
	global_load_dwordx4 v[54:57], v[62:63], off offset:1024 nt
	global_load_dwordx4 v[58:61], v[62:63], off offset:2048 nt
	s_nop 0
	global_load_dwordx4 v[62:65], v[62:63], off offset:3072 nt
	s_branch .LBB0_104
